# XCD-local barriers at merge/w_out/x-attn/dense-up seams guarded by a runtime placement check; o_x written over q_x in place
# speedup vs baseline: 1.0171x; 1.0158x over previous
; #define LAS __attribute__((address_space(3)))
; __device__ __forceinline__ unsigned xb_add(unsigned* p, unsigned v) { return __hip_atomic_fetch_add(p, v, __ATOMIC_RELAXED, __HIP_MEMORY_SCOPE_AGENT); }
; __device__ __forceinline__ unsigned xb_xcc_id() { return (unsigned)__builtin_amdgcn_s_getreg((3 << 11) | 20) & 0xFu; }
; __device__ __forceinline__ XcdBarrier xcd_barrier_post(unsigned* bar, volatile LAS unsigned* st) {
;     XcdBarrier b; b.bar = bar; b.x = xb_xcc_id(); b.st = st; b.wave = __builtin_amdgcn_readfirstlane((int)threadIdx.x >> 6);
;     if (threadIdx.x == 0) (void)xb_add(&bar[XB_XCNT(b.x)], 1u);
;     return b;
; __global__ void __launch_bounds__(NTHREADS, 2) mk_fwd(Params P) {
;     ...
;     Frame F; F.lds = (LAS unsigned char*)lds_raw; F.tid = threadIdx.x; F.lane = F.tid & 63; F.wave = __builtin_amdgcn_readfirstlane(F.tid >> 6); F.G = gridDim.x; F.bid = blockIdx.x; F.ws = P.ws;
;     volatile LAS unsigned* MISC = (volatile LAS unsigned*)(F.lds + MISC_OFF);
;     if (F.tid < 32) MISC[F.tid] = 0u;
;     __syncthreads();
;     unsigned* ctl = (unsigned*)(P.ws + WS_CTL);
;     XcdBarrier bar = xcd_barrier_post(ctl + CW_BAR, MISC + 8);
_ZN2fk6mk_fwdENS_6ParamsE:
	s_mov_b32 s100, 0
	v_readfirstlane_b32 s33, v0
	v_writelane_b32 v253, s2, 0
	s_load_dwordx2 s[2:3], s[0:1], 0x100
	s_load_dword s78, s[0:1], 0x118
	v_cmp_gt_u32_e32 vcc, 32, v0
	s_waitcnt lgkmcnt(0)
	v_writelane_b32 v253, s2, 1
	s_nop 1
	v_writelane_b32 v253, s3, 2
	s_add_u32 s2, s0, 0x118
	s_addc_u32 s3, s1, 0
	v_writelane_b32 v253, s2, 3
	s_nop 1
	v_writelane_b32 v253, s3, 4
	s_and_saveexec_b64 s[2:3], vcc
	v_lshl_add_u32 v1, v0, 2, 0
	v_add_u32_e32 v1, 0x23f80, v1
	v_mov_b32_e32 v2, 0
	ds_write_b32 v1, v2
	s_or_b64 exec, exec, s[2:3]
	s_load_dwordx16 s[4:19], s[0:1], 0x0
	s_load_dwordx2 s[2:3], s[0:1], 0x100
	s_load_dwordx16 s[44:59], s[0:1], 0xc0
	s_waitcnt lgkmcnt(0)
	s_barrier
	v_writelane_b32 v253, s4, 5
	s_add_u32 s2, s2, 0x4000
	s_addc_u32 s3, s3, 0
	v_writelane_b32 v253, s5, 6
	v_writelane_b32 v253, s6, 7
	v_writelane_b32 v253, s7, 8
	v_writelane_b32 v253, s8, 9
	v_writelane_b32 v253, s9, 10
	v_writelane_b32 v253, s10, 11
	v_writelane_b32 v253, s11, 12
	v_writelane_b32 v253, s12, 13
	v_writelane_b32 v253, s13, 14
	v_writelane_b32 v253, s14, 15
	v_writelane_b32 v253, s15, 16
	v_writelane_b32 v253, s16, 17
	v_writelane_b32 v253, s17, 18
	v_writelane_b32 v253, s18, 19
	v_writelane_b32 v253, s19, 20
	s_load_dwordx16 s[4:19], s[0:1], 0x40
	s_waitcnt lgkmcnt(0)
	v_readfirstlane_b32 s39, v0
	v_cmp_eq_u32_e32 vcc, 0, v0
	v_writelane_b32 v253, s4, 21
	s_nop 1
	v_writelane_b32 v253, s5, 22
	v_writelane_b32 v253, s6, 23
	v_writelane_b32 v253, s7, 24
	v_writelane_b32 v253, s8, 25
	v_writelane_b32 v253, s9, 26
	v_writelane_b32 v253, s10, 27
	v_writelane_b32 v253, s11, 28
	v_writelane_b32 v253, s12, 29
	v_writelane_b32 v253, s13, 30
	v_writelane_b32 v253, s14, 31
	v_writelane_b32 v253, s15, 32
	v_writelane_b32 v253, s16, 33
	v_writelane_b32 v253, s17, 34
	v_writelane_b32 v253, s18, 35
	v_writelane_b32 v253, s19, 36
	s_load_dwordx16 s[4:19], s[0:1], 0x80
	s_waitcnt lgkmcnt(0)
	v_writelane_b32 v253, s4, 37
	s_nop 1
	v_writelane_b32 v253, s5, 38
	v_writelane_b32 v253, s6, 39
	v_writelane_b32 v253, s7, 40
	v_writelane_b32 v253, s8, 41
	v_writelane_b32 v253, s9, 42
	v_writelane_b32 v253, s10, 43
	v_writelane_b32 v253, s11, 44
	v_writelane_b32 v253, s12, 45
	v_writelane_b32 v253, s13, 46
	v_writelane_b32 v253, s14, 47
	v_writelane_b32 v253, s15, 48
	v_writelane_b32 v253, s16, 49
	v_writelane_b32 v253, s17, 50
	v_writelane_b32 v253, s18, 51
	v_writelane_b32 v253, s19, 52
	v_writelane_b32 v253, s2, 53
	s_getreg_b32 s7, hwreg(HW_REG_XCC_ID, 0, 4)
	s_mov_b32 s6, 0
	v_writelane_b32 v253, s3, 54
	s_and_saveexec_b64 s[2:3], vcc
	s_cbranch_execz .LBB0_5
	s_mov_b64 s[4:5], exec
	v_mbcnt_lo_u32_b32 v0, s4, 0
	v_mbcnt_hi_u32_b32 v0, s5, v0
	v_cmp_eq_u32_e32 vcc, 0, v0
	s_and_b64 s[8:9], exec, vcc
	s_mov_b64 exec, s[8:9]
	s_cbranch_execz .LBB0_5
	s_lshl_b32 s7, s7, 8
	s_bcnt1_i32_b64 s4, s[4:5]
	s_and_b32 s7, s7, 0xf00
	v_mov_b32_e32 v1, s4
	v_readlane_b32 s4, v253, 53
	v_mov_b32_e32 v0, s7
	v_readlane_b32 s5, v253, 54
	s_nop 4
	global_atomic_add v0, v1, s[4:5] offset:1024
	v_readlane_b32 s8, v253, 0
	s_lshr_b32 s9, s7, 8
	s_and_b32 s8, s8, 7
	s_lshl_b32 s9, 1, s9
	s_lshl_b32 s8, s8, 2
	v_mov_b32_e32 v2, s8
	v_mov_b32_e32 v3, s9
	global_atomic_or v2, v3, s[4:5] offset:64

; __device__ __forceinline__ u64_t* ssq_ptr(unsigned char* ws, int v) { return (u64_t*)(ws + CTL_SSQ) + (size_t)v * NTOK; }
; #define OPAQUE_WS() unsigned char* ws = P.ws; asm volatile("" : "+s"(ws)); F.ws = ws; F.tid = fresh_tid(F.wave); asm volatile("" : "+v"(F.tid)); F.lane = F.tid & 63; int c = F.bid; asm volatile("" : "+s"(c))
; #define REP_BEGIN(k) for (int rep_ = 0, nrep_ = ((k) >= PROBE_LO && (k) < PROBE_HI) ? PROBE_N : 0; rep_ <= nrep_; ++rep_) { const bool rerun = PROBE_AFTER ? (rep_ > 0) : (rep_ < nrep_), dry = rerun && PROBE_DRY_;
; __global__ void __launch_bounds__(NTHREADS, 2) mk_fwd(Params P) {
;     ...
; #pragma unroll 1
;     for (int l = 0; l < DEPTH; ++l) {
;         const int pb = 1 + 9 * l;
;         if (PH_EN(0) && IN(pb + 0)) { REP_BEGIN(pb + 0) OPAQUE_WS(); int lq = l; asm volatile("" : "+s"(lq));
;             if (lq == 0 && !rerun) { phase_dense_w13_b(F, P); xcd_barrier(bar); }
;             if (lq > 0) {
;                 { const int gw = F.bid * NWAVES + F.wave, NGW = F.G * NWAVES; const u64_t* ssq = ssq_ptr(ws, 3 * lq); float* rsq = (float*)(ws + WS_RSQA);
;                   quant_pass((const bf16_t*)(ws + WS_XB), ws + AR_XQA, rsq, ssq, gw, NGW, F.lane, dry); }
;                 xcd_barrier(bar);
;             }
;             { Sched2D Sg{(const char*)(ws + AR_XQA), (const char*)(ws + WB_WIN + lq * SZ_WIN), NTOK / 256, OFF_GL / 256, D / 2, G, c, 0, (NTOK / 256) * (OFF_GL / 256)};
;               EpiIn E{ws, P, lq, dry, rerun};
;               pg8::gemm_phase<EpiIn, Sched2D, true, true, true>(F.lds, D / 2, Sg, E, F.wave); }
.LBB0_223:
	s_or_b64 exec, exec, s[30:31]
	v_readlane_b32 s100, v253, 53
	v_readlane_b32 s101, v253, 54
	v_mov_b32_e32 v8, 0
	s_nop 4
	global_load_dwordx4 v[0:3], v8, s[100:101] offset:64 sc1
	global_load_dwordx4 v[4:7], v8, s[100:101] offset:80 sc1
	s_waitcnt vmcnt(0)
	v_bcnt_u32_b32 v8, v0, 0
	v_bcnt_u32_b32 v8, v1, v8
	v_bcnt_u32_b32 v8, v2, v8
	v_bcnt_u32_b32 v8, v3, v8
	v_bcnt_u32_b32 v8, v4, v8
	v_bcnt_u32_b32 v8, v5, v8
	v_bcnt_u32_b32 v8, v6, v8
	v_bcnt_u32_b32 v8, v7, v8
	v_min_u32_e32 v0, v0, v1
	v_min_u32_e32 v2, v2, v3
	v_min_u32_e32 v4, v4, v5
	v_min_u32_e32 v6, v6, v7
	v_min3_u32 v0, v0, v2, v4
	v_min_u32_e32 v0, v0, v6
	v_readfirstlane_b32 s100, v8
	v_readfirstlane_b32 s101, v0
	s_cmp_eq_u32 s100, 8
	s_cselect_b32 s100, 1, 0
	s_cmp_lg_u32 s101, 0
	s_cselect_b32 s100, s100, 0
	s_cmpk_eq_i32 s78, 0x100
	s_cselect_b32 s100, s100, 0
	s_lshl_b32 s0, s38, 14
	s_add_i32 s0, s0, 0
	s_cmpk_lt_i32 s96, 0xe00
	v_writelane_b32 v254, s0, 28
	s_cselect_b64 s[0:1], -1, 0
	v_writelane_b32 v254, s0, 29
	s_cmpk_lt_i32 s96, 0x700
	s_mov_b32 s93, 0
	v_writelane_b32 v254, s1, 30
	s_cselect_b64 s[0:1], -1, 0
	v_writelane_b32 v254, s0, 31
	s_cmpk_lt_i32 s96, 0x1700
	s_movk_i32 s84, 0x4000
	v_writelane_b32 v254, s1, 32
	s_cselect_b64 s[0:1], -1, 0
	v_writelane_b32 v254, s0, 33
	s_lshl_b32 s2, s78, 5
	s_ashr_i32 s95, s78, 31
	v_writelane_b32 v254, s1, 34
	s_bfe_u32 s0, s33, 0x20006
	v_writelane_b32 v254, s0, 19
	s_lshl_b32 s0, s0, 7
	s_cmpk_lt_i32 s96, 0x4000
	v_writelane_b32 v254, s0, 35
	s_cselect_b64 s[0:1], -1, 0
	s_cmpk_eq_i32 s78, 0x100
	s_cselect_b64 s[4:5], -1, 0
	v_writelane_b32 v254, s4, 10
	v_mov_b32_e32 v113, 0
	v_mov_b32_e32 v248, 1
	v_writelane_b32 v254, s5, 11
	s_add_u32 s4, s86, 0x1000
	s_addc_u32 s5, s87, 0
	v_writelane_b32 v254, s4, 36
	s_cmpk_lt_i32 s96, 0x1c00
	s_mov_b32 s86, s2
	v_writelane_b32 v254, s5, 37
	s_cselect_b64 s[2:3], -1, 0
	v_writelane_b32 v254, s2, 38
	s_cmp_lt_i32 s96, 0xa800
	v_readlane_b32 s4, v253, 0
	v_writelane_b32 v254, s3, 39
	s_cselect_b64 s[2:3], -1, 0
	v_writelane_b32 v254, s2, 40
	s_ashr_i32 s97, s96, 31
	s_ashr_i32 s87, s86, 31
	v_writelane_b32 v254, s3, 41
	s_lshl_b32 s2, s4, 8
	s_lshl_b32 s3, s38, 5
	s_add_i32 s5, s2, s3
	s_lshl_b32 s2, s4, 7
	s_lshl_b32 s3, s38, 4
	s_add_i32 s6, s2, s3
	s_lshl_b32 s2, s4, 4
	s_lshl_b32 s3, s38, 1
	s_add_i32 s7, s2, s3
	s_lshl_b32 s2, s4, 10
	s_lshl_b32 s3, s38, 7
	s_add_i32 s2, s2, s3
	v_writelane_b32 v254, s2, 42
	s_lshl_b32 s2, s4, 11
	s_lshl_b32 s3, s38, 8
	s_add_i32 s2, s2, s3
	v_writelane_b32 v254, s2, 43
	v_writelane_b32 v254, s5, 44
	s_or_b32 s2, s5, 3
	v_writelane_b32 v254, s2, 45
	s_or_b32 s2, s6, 3
	v_writelane_b32 v254, s2, 46
	s_or_b32 s2, s6, 2
	v_writelane_b32 v254, s2, 47
	v_writelane_b32 v254, s6, 48
	s_or_b32 s2, s6, 1
	v_writelane_b32 v254, s2, 49
	s_lshl_b32 s2, s4, 6
	s_lshl_b32 s3, s38, 3
	s_add_i32 s2, s2, s3
	s_add_i32 s2, s2, 0x7ffff200
	v_writelane_b32 v254, s2, 50
	s_lshl_b32 s2, s78, 6
	v_writelane_b32 v254, s2, 51
	s_lshl_b32 s2, s38, 6
	s_add_i32 s2, s36, s2
	v_writelane_b32 v254, s2, 52
	s_sub_i32 s2, 0xa7ff, s96
	s_lshl_b32 s3, s2, 5
	v_writelane_b32 v254, s3, 53
	v_writelane_b32 v254, s2, 54
	s_lshl_b32 s2, s2, 1
	v_writelane_b32 v254, s2, 55
	v_writelane_b32 v254, s7, 56
	s_or_b32 s2, s7, 1
	v_writelane_b32 v254, s2, 57
	s_lshl_b64 s[2:3], s[96:97], 12
	v_writelane_b32 v254, s2, 58
	s_lshl_b32 s75, s78, 8
	s_lshl_b32 s79, s78, 7
	v_writelane_b32 v254, s3, 59
	s_lshl_b64 s[2:3], s[86:87], 12
	v_writelane_b32 v254, s2, 60
	s_lshl_b32 s81, s78, 4
	s_lshl_b32 s82, s78, 10
	s_lshl_b32 s89, s78, 11
	v_writelane_b32 v254, s3, 61
	s_lshl_b64 s[2:3], s[96:97], 11
	s_add_u32 s2, s2, 0x4f00400
	v_writelane_b32 v254, s2, 62
	s_addc_u32 s2, s3, 0
	v_writelane_b32 v254, s2, 63
	s_mov_b32 s2, s96
	v_writelane_b32 v255, s2, 0
	s_xor_b64 s[0:1], s[0:1], -1
	s_movk_i32 s97, 0xe00
	v_writelane_b32 v255, s3, 1
	s_add_i32 s2, s96, s76
	s_ashr_i32 s3, s2, 31
	s_lshl_b64 s[2:3], s[2:3], 12
	v_writelane_b32 v255, s2, 2
	s_movk_i32 s96, 0x5c00
	s_mov_b32 s73, 0x8000
	v_writelane_b32 v255, s3, 3
	s_add_i32 s2, 0, 0x23fa0
	v_writelane_b32 v254, s2, 8
	s_add_i32 s2, 0, 0x23fa4
	v_writelane_b32 v255, s0, 4
	v_writelane_b32 v254, s2, 9
	v_mov_b32_e32 v249, 0x358637bd
	v_writelane_b32 v255, s1, 5
	s_add_i32 s0, 0, 0x11000
	v_writelane_b32 v254, s0, 13
	s_add_i32 s0, 0, 0x1115c
	v_writelane_b32 v254, s0, 12
	s_add_i32 s0, 0, 0x23fc0
	v_writelane_b32 v254, s0, 15
	s_add_i32 s0, 0, 0x23fd0
	v_writelane_b32 v254, s0, 16
	s_add_i32 s0, 0, 0x23fdc
	v_writelane_b32 v255, s0, 6
	s_lshl_b64 s[0:1], s[86:87], 11
	v_writelane_b32 v255, s0, 7
	s_mov_b32 s92, 0xa000
	v_mov_b32_e32 v250, 0x1000
	v_writelane_b32 v255, s1, 8
	s_mov_b32 s0, s76
	v_writelane_b32 v255, s0, 9
	v_mbcnt_hi_u32_b32 v251, -1, v82
	v_mov_b32_e32 v252, 0xf149f2ca
	v_writelane_b32 v255, s1, 10
	s_mov_b32 s0, s86
	v_writelane_b32 v255, s0, 11
	v_mov_b32_e32 v164, 0x43e00000
	s_movk_i32 s85, 0x80
	v_writelane_b32 v255, s1, 12
	v_writelane_b32 v255, s75, 13
	v_writelane_b32 v255, s79, 14
	v_writelane_b32 v255, s81, 15
	v_writelane_b32 v255, s82, 16
	s_mov_b32 s60, 0xc000
	s_mov_b32 s61, 0xe000
	s_mov_b32 s80, 0x41000000
	s_mov_b32 s70, 0xc3e00000
	s_mov_b64 s[34:35], -1
	s_mov_b64 s[66:67], 0x2000
	s_mov_b32 s36, s93
	v_writelane_b32 v254, s95, 14
	v_writelane_b32 v255, s89, 17
	s_waitcnt lgkmcnt(0)
	s_barrier
	s_branch .LBB0_227

; __device__ __forceinline__ int fresh_tid(int wave) { return wave * 64 + fresh_lane(); }
; __device__ __forceinline__ unsigned xb_ld(unsigned* p)              { return __hip_atomic_load(p, __ATOMIC_RELAXED, __HIP_MEMORY_SCOPE_AGENT); }
; __device__ __forceinline__ unsigned xb_add(unsigned* p, unsigned v) { return __hip_atomic_fetch_add(p, v, __ATOMIC_RELAXED, __HIP_MEMORY_SCOPE_AGENT); }
; __device__ __forceinline__ unsigned xb_xcc_id() { return (unsigned)__builtin_amdgcn_s_getreg((3 << 11) | 20) & 0xFu; }
; #define XB_SPIN(cond, bar) do { unsigned _sp = 0; while (cond) { __builtin_amdgcn_s_sleep(1); \
;     if ((++_sp & 255u) == 0u) { if (xb_ld(&(bar)[XB_TMO])) break; if (_sp > XB_SPIN_CAP) { atomicAdd(&(bar)[XB_TMO], 1u); break; } } } } while (0)
; __device__ __forceinline__ void xcd_barrier(const XcdBarrier& b) {
;     asm volatile("s_waitcnt vmcnt(0)" ::: "memory");
;     __syncthreads();
;     if (fresh_tid(b.wave) == 0) {
;         unsigned* bar = b.bar; asm volatile("" : "+s"(bar));
;         __builtin_amdgcn_s_waitcnt(0);
;         const unsigned bx = xb_xcc_id();
;         unsigned nloc = b.st[0], nx = b.st[1];
;         if (nloc == 0u) { xcd_barrier_complete(bar, bx, nloc, nx); b.st[0] = nloc; b.st[1] = nx; }
;         const unsigned old = xb_add(&bar[XB_XSUB(bx)], 1u);
;         const unsigned gen = old / nloc;
;         if (old + 1u == (gen + 1u) * nloc) {
;             __builtin_amdgcn_fence(__ATOMIC_RELEASE, "agent");
;             asm volatile("s_waitcnt vmcnt(0)" ::: "memory");
;             const unsigned og = xb_add(&bar[XB_TOP], 1u);
;             const unsigned tg = og / nx;
;             if (og + 1u == (tg + 1u) * nx) xb_add(&bar[XB_TOPGEN], 1u);
;             else XB_SPIN(xb_ld(&bar[XB_TOPGEN]) == tg, bar);
;             __builtin_amdgcn_fence(__ATOMIC_ACQUIRE, "agent");
;             xb_add(&bar[XB_XGEN(bx)], 1u);
;             asm volatile("s_waitcnt vmcnt(0)" ::: "memory");
;         } else {
;             XB_SPIN(xb_ld(&bar[XB_XGEN(bx)]) == gen, bar);
;             __builtin_amdgcn_fence(__ATOMIC_ACQUIRE, "agent");
;             asm volatile("s_waitcnt vmcnt(0)" ::: "memory");
;         }
.LBB0_1023:
	s_mov_b32 s0, s93
	s_waitcnt vmcnt(0)
	s_waitcnt lgkmcnt(0)
	s_barrier
	s_nop 0
	v_mbcnt_lo_u32_b32 v0, -1, s0
	v_mbcnt_hi_u32_b32 v0, -1, v0
	v_readlane_b32 s0, v254, 17
	s_nop 1
	v_cmp_eq_u32_e32 vcc, s0, v0
	s_and_saveexec_b64 s[0:1], vcc
	s_cbranch_execz .LBB0_1067
	s_bitcmp1_b32 s100, 0
	s_cbranch_scc0 .Llb_mg_glob
	v_readlane_b32 s2, v253, 53
	v_readlane_b32 s3, v253, 54
	v_readlane_b32 s4, v253, 0
	v_mov_b32_e32 v1, 1
	s_and_b32 s4, s4, 7
	s_lshl_b32 s4, s4, 8
	s_addk_i32 s4, 0x480
	v_mov_b32_e32 v0, s4
	s_waitcnt vmcnt(0) lgkmcnt(0)
	global_atomic_add v2, v0, v1, s[2:3] sc0
	s_mov_b32 s5, 0
	s_waitcnt vmcnt(0)
	v_or_b32_e32 v2, 31, v2
	v_add_u32_e32 v2, 1, v2
.Llb_mg_spin:
	global_load_dword v3, v0, s[2:3] sc1
	s_waitcnt vmcnt(0)
	v_sub_u32_e32 v3, v3, v2
	v_cmp_gt_i32_e32 vcc, 0, v3
	s_cbranch_vccz .Llb_mg_done
	s_sleep 1
	s_add_i32 s5, s5, 1
	s_cmp_lt_u32 s5, 0x100000
	s_cbranch_scc1 .Llb_mg_spin
.Llb_mg_done:
	buffer_inv sc1
	s_branch .LBB0_1067
.Llb_mg_glob:
	v_readlane_b32 s2, v253, 53
	v_readlane_b32 s5, v254, 8
	v_readlane_b32 s3, v253, 54
	s_waitcnt vmcnt(0) expcnt(0) lgkmcnt(0)
	v_mov_b32_e32 v0, s5
	s_getreg_b32 s4, hwreg(HW_REG_XCC_ID, 0, 4)
	ds_read_b32 v2, v0
	v_readlane_b32 s5, v254, 9
	s_and_b32 s33, s4, 15
	s_waitcnt lgkmcnt(0)
	v_cmp_ne_u32_e32 vcc, 0, v2
	v_mov_b32_e32 v0, s5
	ds_read_b32 v0, v0
	s_cbranch_vccnz .LBB0_1038
	v_readlane_b32 s4, v253, 3
	v_readlane_b32 s5, v253, 4
	s_load_dwordx2 s[8:9], s[4:5], 0x4
	s_add_u32 s4, s2, 0x1000
	s_addc_u32 s5, s3, 0
	s_add_u32 s6, s2, 0x1100
	s_addc_u32 s7, s3, 0
	s_waitcnt lgkmcnt(0)
	s_mul_i32 s30, s8, s78
	s_add_u32 s8, s2, 0x1200
	s_mul_i32 s30, s30, s9
	s_addc_u32 s9, s3, 0
	s_add_u32 s10, s2, 0x1300
	s_addc_u32 s11, s3, 0
	s_mov_b32 s31, 1
	s_mov_b64 s[12:13], 0
	s_branch .LBB0_1028

; __global__ void __launch_bounds__(NTHREADS, 2) mk_fwd(Params P) {
;     ...
;             att::XArgs A{(const bf16_t*)(ws + AR_QX), (const bf16_t*)(ws + WS_KXV) + (size_t)lq * B * MEM * 1024, (bf16_t*)(ws + AR_OX), P.in[20] + lq * XHD, dry};
;             for (int u = c, rnd = 0; u < B * XH * (S / 256); u += G, ++rnd) { int qt = u & 15, h = (u >> 4) & 3, b = u >> 6;
;                 if (G == 256) { const int idx = rnd * 32 + (c >> 3), bh = (c & 7) * 4 + (idx >> 4); qt = idx & 15; h = bh & 3; b = bh >> 2; }
;                 att::xattn_unit(A, b, h, qt, F.lds, F.wave); }
.LBB0_1221:
	s_or_b64 exec, exec, s[0:1]
	v_readlane_b32 s2, v253, 1
	v_readlane_b32 s3, v253, 2
	s_mov_b32 s0, s93
	s_waitcnt lgkmcnt(0)
	s_barrier
	v_readlane_b32 s18, v253, 0
	v_mbcnt_lo_u32_b32 v0, -1, s0
	v_mbcnt_hi_u32_b32 v0, -1, v0
	v_add_u32_e32 v0, s94, v0
	v_readlane_b32 s4, v255, 20
	s_cmpk_gt_i32 s18, 0x1ff
	v_readlane_b32 s5, v255, 21
	s_cbranch_scc1 .LBB0_1237
	s_add_u32 s0, s2, 0x8f00000
	s_addc_u32 s1, s3, 0
	s_ashr_i32 s5, s4, 31
	s_lshl_b64 s[6:7], s[4:5], 22
	s_add_u32 s19, s2, s6
	s_addc_u32 s20, s3, s7
	s_add_u32 s21, s19, 0x700000
	s_addc_u32 s22, s20, 0
	s_add_u32 s23, s2, 0x8f00000
	s_addc_u32 s24, s3, 0
	s_lshl_b32 s2, s4, 7
	v_readlane_b32 s36, v253, 37
	s_ashr_i32 s3, s2, 31
	v_readlane_b32 s44, v253, 45
	v_readlane_b32 s45, v253, 46
	s_lshl_b64 s[2:3], s[2:3], 2
	v_readlane_b32 s46, v253, 47
	v_readlane_b32 s47, v253, 48
	s_mov_b64 s[8:9], s[44:45]
	s_add_u32 s2, s8, s2
	s_addc_u32 s3, s9, s3
	s_lshl_b32 s4, s18, 2
	s_ashr_i32 s25, s18, 3
	s_and_b32 s26, s4, 28
	s_add_u32 s6, s19, 0x740400
	s_addc_u32 s7, s20, 0
	s_mov_b32 s27, 0
	v_readlane_b32 s37, v253, 38
	v_readlane_b32 s38, v253, 39
	v_readlane_b32 s39, v253, 40
	v_readlane_b32 s40, v253, 41
	v_readlane_b32 s41, v253, 42
	v_readlane_b32 s42, v253, 43
	v_readlane_b32 s43, v253, 44
	v_readlane_b32 s48, v253, 49
	v_readlane_b32 s49, v253, 50
	v_readlane_b32 s50, v253, 51
	v_readlane_b32 s51, v253, 52
	s_mov_b64 s[10:11], s[46:47]
	s_branch .LBB0_1224

; __device__ __forceinline__ int fresh_tid(int wave) { return wave * 64 + fresh_lane(); }
; __device__ __forceinline__ unsigned xb_add(unsigned* p, unsigned v) { return __hip_atomic_fetch_add(p, v, __ATOMIC_RELAXED, __HIP_MEMORY_SCOPE_AGENT); }
; __device__ __forceinline__ unsigned xb_xcc_id() { return (unsigned)__builtin_amdgcn_s_getreg((3 << 11) | 20) & 0xFu; }
; __device__ __forceinline__ void xcd_barrier(const XcdBarrier& b) {
;     asm volatile("s_waitcnt vmcnt(0)" ::: "memory");
;     __syncthreads();
;     if (fresh_tid(b.wave) == 0) {
;         unsigned* bar = b.bar; asm volatile("" : "+s"(bar));
;         __builtin_amdgcn_s_waitcnt(0);
;         const unsigned bx = xb_xcc_id();
;         unsigned nloc = b.st[0], nx = b.st[1];
;         if (nloc == 0u) { xcd_barrier_complete(bar, bx, nloc, nx); b.st[0] = nloc; b.st[1] = nx; }
;         const unsigned old = xb_add(&bar[XB_XSUB(bx)], 1u);
;         const unsigned gen = old / nloc;
;         if (old + 1u == (gen + 1u) * nloc) {
.LBB0_1237:
	s_mov_b32 s0, s93
	s_waitcnt lgkmcnt(0)
	s_barrier
	s_waitcnt vmcnt(0)
	s_barrier
	s_nop 0
	v_mbcnt_lo_u32_b32 v0, -1, s0
	v_mbcnt_hi_u32_b32 v0, -1, v0
	v_readlane_b32 s0, v254, 17
	s_nop 1
	v_cmp_eq_u32_e32 vcc, s0, v0
	s_and_saveexec_b64 s[0:1], vcc
	s_cbranch_execz .LBB0_1281
	s_bitcmp1_b32 s100, 0
	s_cbranch_scc0 .Llb_x2_glob
	v_readlane_b32 s2, v253, 53
	v_readlane_b32 s3, v253, 54
	v_readlane_b32 s4, v253, 0
	v_mov_b32_e32 v1, 1
	s_and_b32 s4, s4, 7
	s_lshl_b32 s4, s4, 8
	s_addk_i32 s4, 0x480
	v_mov_b32_e32 v0, s4
	s_waitcnt vmcnt(0) lgkmcnt(0)
	global_atomic_add v2, v0, v1, s[2:3] sc0
	s_mov_b32 s5, 0
	s_waitcnt vmcnt(0)
	v_or_b32_e32 v2, 31, v2
	v_add_u32_e32 v2, 1, v2

; #define OPAQUE_WS() unsigned char* ws = P.ws; asm volatile("" : "+s"(ws)); F.ws = ws; F.tid = fresh_tid(F.wave); asm volatile("" : "+v"(F.tid)); F.lane = F.tid & 63; int c = F.bid; asm volatile("" : "+s"(c))
; #define REP_BEGIN(k) for (int rep_ = 0, nrep_ = ((k) >= PROBE_LO && (k) < PROBE_HI) ? PROBE_N : 0; rep_ <= nrep_; ++rep_) { const bool rerun = PROBE_AFTER ? (rep_ > 0) : (rep_ < nrep_), dry = rerun && PROBE_DRY_;
; __global__ void __launch_bounds__(NTHREADS, 2) mk_fwd(Params P) {
;     ...
;         if (PH_EN(6) && IN(pb + 6)) { REP_BEGIN(pb + 6) OPAQUE_WS(); int lq = l; asm volatile("" : "+s"(lq));
;             Sched2D Sg{(const char*)(ws + AR_OX), (const char*)(ws + WB_WXO + lq * SZ_WXO), NTOK / 256, D / 256, XW, G, c, 0, (NTOK / 256) * (D / 256)};
;             EpiRes E{ws, 3 * lq + 2, dry};
;             pg8::gemm_phase<EpiRes, Sched2D>(F.lds, XW, Sg, E, F.wave);
.LBB0_1281:
	s_or_b64 exec, exec, s[0:1]
	v_readlane_b32 s4, v253, 1
	v_readlane_b32 s5, v253, 2
	s_mov_b32 s0, 0
	s_waitcnt lgkmcnt(0)
	s_barrier
	v_readlane_b32 s28, v253, 0
	v_mbcnt_lo_u32_b32 v0, -1, s0
	v_mbcnt_hi_u32_b32 v0, -1, v0
	v_readlane_b32 s0, v255, 20
	v_add_u32_e32 v0, s94, v0
	v_readlane_b32 s1, v255, 21
	s_add_u32 s29, s4, 0x8f00000
	s_addc_u32 s30, s5, 0
	s_ashr_i32 s1, s0, 31
	s_mov_b32 s10, s0
	s_lshl_b64 s[0:1], s[0:1], 20
	s_add_u32 s0, s4, s0
	s_addc_u32 s1, s5, s1
	s_add_u32 s31, s0, 0x3800000
	s_mov_b32 s0, s93
	s_addc_u32 s33, s1, 0
	v_mbcnt_lo_u32_b32 v0, -1, s0
	v_mbcnt_hi_u32_b32 v0, -1, v0
	v_add_u32_e32 v0, s94, v0
	s_cmpk_lt_i32 s28, 0x200
	s_cselect_b64 s[0:1], -1, 0
	s_cmpk_gt_i32 s28, 0x1ff
	v_readfirstlane_b32 s6, v0
	s_cbranch_scc1 .LBB0_1287
	s_ashr_i32 s2, s28, 31
	s_lshr_b32 s2, s2, 29
	s_add_i32 s7, s28, s2
	s_and_b32 s2, s7, -8
	s_sub_i32 s8, s28, s2
	s_cmp_gt_i32 s8, -1
	s_mov_b64 s[2:3], -1
	s_cbranch_scc0 .LBB0_1284
	s_lshl_b32 s9, s8, 6
	s_mov_b64 s[2:3], 0

; __device__ __forceinline__ int fresh_tid(int wave) { return wave * 64 + fresh_lane(); }
; __device__ __forceinline__ unsigned xb_ld(unsigned* p)              { return __hip_atomic_load(p, __ATOMIC_RELAXED, __HIP_MEMORY_SCOPE_AGENT); }
; __device__ __forceinline__ unsigned xb_add(unsigned* p, unsigned v) { return __hip_atomic_fetch_add(p, v, __ATOMIC_RELAXED, __HIP_MEMORY_SCOPE_AGENT); }
; __device__ __forceinline__ unsigned xb_xcc_id() { return (unsigned)__builtin_amdgcn_s_getreg((3 << 11) | 20) & 0xFu; }
; #define XB_SPIN(cond, bar) do { unsigned _sp = 0; while (cond) { __builtin_amdgcn_s_sleep(1); \
;     if ((++_sp & 255u) == 0u) { if (xb_ld(&(bar)[XB_TMO])) break; if (_sp > XB_SPIN_CAP) { atomicAdd(&(bar)[XB_TMO], 1u); break; } } } } while (0)
; __device__ __forceinline__ void xcd_barrier(const XcdBarrier& b) {
;     asm volatile("s_waitcnt vmcnt(0)" ::: "memory");
;     __syncthreads();
;     if (fresh_tid(b.wave) == 0) {
;         unsigned* bar = b.bar; asm volatile("" : "+s"(bar));
;         __builtin_amdgcn_s_waitcnt(0);
;         const unsigned bx = xb_xcc_id();
;         unsigned nloc = b.st[0], nx = b.st[1];
;         if (nloc == 0u) { xcd_barrier_complete(bar, bx, nloc, nx); b.st[0] = nloc; b.st[1] = nx; }
;         const unsigned old = xb_add(&bar[XB_XSUB(bx)], 1u);
;         const unsigned gen = old / nloc;
;         if (old + 1u == (gen + 1u) * nloc) {
;             __builtin_amdgcn_fence(__ATOMIC_RELEASE, "agent");
;             asm volatile("s_waitcnt vmcnt(0)" ::: "memory");
;             const unsigned og = xb_add(&bar[XB_TOP], 1u);
;             const unsigned tg = og / nx;
;             if (og + 1u == (tg + 1u) * nx) xb_add(&bar[XB_TOPGEN], 1u);
;             else XB_SPIN(xb_ld(&bar[XB_TOPGEN]) == tg, bar);
;             __builtin_amdgcn_fence(__ATOMIC_ACQUIRE, "agent");
;             xb_add(&bar[XB_XGEN(bx)], 1u);
;             asm volatile("s_waitcnt vmcnt(0)" ::: "memory");
;         } else {
;             XB_SPIN(xb_ld(&bar[XB_XGEN(bx)]) == gen, bar);
;             __builtin_amdgcn_fence(__ATOMIC_ACQUIRE, "agent");
;             asm volatile("s_waitcnt vmcnt(0)" ::: "memory");
;         }
.LBB0_1774:
	s_mov_b32 s0, s93
	s_waitcnt vmcnt(0)
	s_waitcnt lgkmcnt(0)
	s_barrier
	s_nop 0
	v_mbcnt_lo_u32_b32 v0, -1, s0
	v_mbcnt_hi_u32_b32 v0, -1, v0
	v_readlane_b32 s0, v254, 17
	s_nop 1
	v_cmp_eq_u32_e32 vcc, s0, v0
	s_and_saveexec_b64 s[30:31], vcc
	s_cbranch_execz .LBB0_1818
	s_bitcmp1_b32 s100, 0
	s_cbranch_scc0 .Llb_f1_glob
	v_readlane_b32 s34, v253, 53
	v_readlane_b32 s35, v253, 54
	v_readlane_b32 s0, v253, 0
	v_mov_b32_e32 v1, 1
	s_and_b32 s0, s0, 7
	s_lshl_b32 s0, s0, 8
	s_addk_i32 s0, 0x480
	v_mov_b32_e32 v0, s0
	s_waitcnt vmcnt(0) lgkmcnt(0)
	global_atomic_add v2, v0, v1, s[34:35] sc0
	s_mov_b32 s1, 0
	s_waitcnt vmcnt(0)
	v_or_b32_e32 v2, 31, v2
	v_add_u32_e32 v2, 1, v2
.Llb_f1_spin:
	global_load_dword v3, v0, s[34:35] sc1
	s_waitcnt vmcnt(0)
	v_sub_u32_e32 v3, v3, v2
	v_cmp_gt_i32_e32 vcc, 0, v3
	s_cbranch_vccz .Llb_f1_done
	s_sleep 1
	s_add_i32 s1, s1, 1
	s_cmp_lt_u32 s1, 0x100000
	s_cbranch_scc1 .Llb_f1_spin

; __global__ void __launch_bounds__(NTHREADS, 2) mk_fwd(Params P) {
	.amdhsa_kernel _ZN2fk6mk_fwdENS_6ParamsE
		.amdhsa_group_segment_fixed_size 0
		.amdhsa_private_segment_fixed_size 0
		.amdhsa_kernarg_size 536
		.amdhsa_user_sgpr_count 2
		.amdhsa_user_sgpr_dispatch_ptr 0
		.amdhsa_user_sgpr_queue_ptr 0
		.amdhsa_user_sgpr_kernarg_segment_ptr 1
		.amdhsa_user_sgpr_dispatch_id 0
		.amdhsa_user_sgpr_kernarg_preload_length 0
		.amdhsa_user_sgpr_kernarg_preload_offset 0
		.amdhsa_user_sgpr_private_segment_size 0
		.amdhsa_uses_dynamic_stack 0
		.amdhsa_enable_private_segment 0
		.amdhsa_system_sgpr_workgroup_id_x 1
		.amdhsa_system_sgpr_workgroup_id_y 0
		.amdhsa_system_sgpr_workgroup_id_z 0
		.amdhsa_system_sgpr_workgroup_info 0
		.amdhsa_system_vgpr_workitem_id 0
		.amdhsa_next_free_vgpr 256
	.amdhsa_next_free_sgpr 102
		.amdhsa_accum_offset 256
		.amdhsa_reserve_vcc 1
		.amdhsa_float_round_mode_32 0
		.amdhsa_float_round_mode_16_64 0
		.amdhsa_float_denorm_mode_32 3
		.amdhsa_float_denorm_mode_16_64 3
		.amdhsa_dx10_clamp 1
		.amdhsa_ieee_mode 1
		.amdhsa_fp16_overflow 0
		.amdhsa_tg_split 0
		.amdhsa_exception_fp_ieee_invalid_op 0
		.amdhsa_exception_fp_denorm_src 0
		.amdhsa_exception_fp_ieee_div_zero 0
		.amdhsa_exception_fp_ieee_overflow 0
		.amdhsa_exception_fp_ieee_underflow 0
		.amdhsa_exception_fp_ieee_inexact 0
		.amdhsa_exception_int_div_zero 0
	.end_amdhsa_kernel

; __global__ void __launch_bounds__(NTHREADS, 2) mk_fwd(Params P) {
amdhsa.kernels:
  - .agpr_count:     0
    .args:
      - .offset:         0
        .size:           280
        .value_kind:     by_value
      - .offset:         280
        .size:           4
        .value_kind:     hidden_block_count_x
      - .offset:         284
        .size:           4
        .value_kind:     hidden_block_count_y
      - .offset:         288
        .size:           4
        .value_kind:     hidden_block_count_z
      - .offset:         292
        .size:           2
        .value_kind:     hidden_group_size_x
      - .offset:         294
        .size:           2
        .value_kind:     hidden_group_size_y
      - .offset:         296
        .size:           2
        .value_kind:     hidden_group_size_z
      - .offset:         298
        .size:           2
        .value_kind:     hidden_remainder_x
      - .offset:         300
        .size:           2
        .value_kind:     hidden_remainder_y
      - .offset:         302
        .size:           2
        .value_kind:     hidden_remainder_z
      - .offset:         320
        .size:           8
        .value_kind:     hidden_global_offset_x
      - .offset:         328
        .size:           8
        .value_kind:     hidden_global_offset_y
      - .offset:         336
        .size:           8
        .value_kind:     hidden_global_offset_z
      - .offset:         344
        .size:           2
        .value_kind:     hidden_grid_dims
      - .offset:         400
        .size:           4
        .value_kind:     hidden_dynamic_lds_size
    .group_segment_fixed_size: 0
    .kernarg_segment_align: 8
    .kernarg_segment_size: 536
    .language:       OpenCL C
    .language_version:
      - 2
      - 0
    .max_flat_workgroup_size: 512
    .name:           _ZN2fk6mk_fwdENS_6ParamsE
    .private_segment_fixed_size: 0
    .sgpr_count:     108
    .sgpr_spill_count: 213
    .symbol:         _ZN2fk6mk_fwdENS_6ParamsE.kd
    .uniform_work_group_size: 1
    .uses_dynamic_stack: false
    .vgpr_count:     256
    .vgpr_spill_count: 0
    .wavefront_size: 64
